# v58 + fox unit prologue: key-bias staging copy issues all loads before one wait; q-row and diagonal-key loads in flight together
# speedup vs baseline: 1.0031x; 1.0005x over previous
.LBB0_270:
	v_cmp_gt_i32_e32 vcc, s35, v96
	s_and_saveexec_b64 s[8:9], vcc
	s_cbranch_execz .LBB0_273
	v_mov_b64_e32 v[0:1], v[136:137]
	v_mov_b32_e32 v36, v96
	global_load_dwordx4 v[4:7], v[0:1], off
	v_lshl_add_u64 v[0:1], v[0:1], 0, s[40:41]
	v_add_u32_e32 v36, 0x200, v36
	v_cmp_le_i32_e32 vcc, s35, v36
	s_andn2_b64 exec, exec, vcc
	global_load_dwordx4 v[8:11], v[0:1], off
	v_lshl_add_u64 v[0:1], v[0:1], 0, s[40:41]
	v_add_u32_e32 v36, 0x200, v36
	v_cmp_le_i32_e32 vcc, s35, v36
	s_andn2_b64 exec, exec, vcc
	global_load_dwordx4 v[12:15], v[0:1], off
	v_lshl_add_u64 v[0:1], v[0:1], 0, s[40:41]
	v_add_u32_e32 v36, 0x200, v36
	v_cmp_le_i32_e32 vcc, s35, v36
	s_andn2_b64 exec, exec, vcc
	global_load_dwordx4 v[16:19], v[0:1], off
	v_lshl_add_u64 v[0:1], v[0:1], 0, s[40:41]
	v_add_u32_e32 v36, 0x200, v36
	v_cmp_le_i32_e32 vcc, s35, v36
	s_andn2_b64 exec, exec, vcc
	global_load_dwordx4 v[20:23], v[0:1], off
	v_lshl_add_u64 v[0:1], v[0:1], 0, s[40:41]
	v_add_u32_e32 v36, 0x200, v36
	v_cmp_le_i32_e32 vcc, s35, v36
	s_andn2_b64 exec, exec, vcc
	global_load_dwordx4 v[24:27], v[0:1], off
	v_lshl_add_u64 v[0:1], v[0:1], 0, s[40:41]
	v_add_u32_e32 v36, 0x200, v36
	v_cmp_le_i32_e32 vcc, s35, v36
	s_andn2_b64 exec, exec, vcc
	global_load_dwordx4 v[28:31], v[0:1], off
	v_lshl_add_u64 v[0:1], v[0:1], 0, s[40:41]
	v_add_u32_e32 v36, 0x200, v36
	v_cmp_le_i32_e32 vcc, s35, v36
	s_andn2_b64 exec, exec, vcc
	global_load_dwordx4 v[32:35], v[0:1], off
	v_lshl_add_u64 v[0:1], v[0:1], 0, s[40:41]
	v_add_u32_e32 v36, 0x200, v36
	v_cmp_le_i32_e32 vcc, s35, v36
	s_andn2_b64 exec, exec, vcc
	s_mov_b64 exec, s[8:9]
	v_cmp_gt_i32_e32 vcc, s35, v96
	s_and_b64 exec, exec, vcc
	v_mov_b32_e32 v2, v227
	v_mov_b32_e32 v36, v96
	s_waitcnt vmcnt(0)
	ds_write_b128 v2, v[4:7]
	v_add_u32_e32 v2, 0x2000, v2
	v_add_u32_e32 v36, 0x200, v36
	v_cmp_le_i32_e32 vcc, s35, v36
	s_andn2_b64 exec, exec, vcc
	ds_write_b128 v2, v[8:11]
	v_add_u32_e32 v2, 0x2000, v2
	v_add_u32_e32 v36, 0x200, v36
	v_cmp_le_i32_e32 vcc, s35, v36
	s_andn2_b64 exec, exec, vcc
	ds_write_b128 v2, v[12:15]
	v_add_u32_e32 v2, 0x2000, v2
	v_add_u32_e32 v36, 0x200, v36
	v_cmp_le_i32_e32 vcc, s35, v36
	s_andn2_b64 exec, exec, vcc
	ds_write_b128 v2, v[16:19]
	v_add_u32_e32 v2, 0x2000, v2
	v_add_u32_e32 v36, 0x200, v36
	v_cmp_le_i32_e32 vcc, s35, v36
	s_andn2_b64 exec, exec, vcc
	ds_write_b128 v2, v[20:23]
	v_add_u32_e32 v2, 0x2000, v2
	v_add_u32_e32 v36, 0x200, v36
	v_cmp_le_i32_e32 vcc, s35, v36
	s_andn2_b64 exec, exec, vcc
	ds_write_b128 v2, v[24:27]
	v_add_u32_e32 v2, 0x2000, v2
	v_add_u32_e32 v36, 0x200, v36
	v_cmp_le_i32_e32 vcc, s35, v36
	s_andn2_b64 exec, exec, vcc
	ds_write_b128 v2, v[28:31]
	v_add_u32_e32 v2, 0x2000, v2
	v_add_u32_e32 v36, 0x200, v36
	v_cmp_le_i32_e32 vcc, s35, v36
	s_andn2_b64 exec, exec, vcc
	ds_write_b128 v2, v[32:35]
	v_add_u32_e32 v2, 0x2000, v2
	v_add_u32_e32 v36, 0x200, v36
	v_cmp_le_i32_e32 vcc, s35, v36
	s_andn2_b64 exec, exec, vcc
.LBB0_273:
	s_or_b64 exec, exec, s[8:9]
	s_and_saveexec_b64 s[8:9], s[6:7]
	v_mov_b32_e32 v0, s66
	ds_write_b64 v0, v[110:111]
	s_or_b64 exec, exec, s[8:9]
	s_lshl_b32 s42, s51, 8
	s_add_u32 s50, s45, s42
	s_addc_u32 s35, s46, 0
	s_mul_i32 s43, s35, 0x1e00
	v_mad_u64_u32 v[0:1], s[8:9], s50, v233, v[126:127]
	v_add_u32_e32 v1, s43, v1
	global_load_dwordx4 v[64:67], v[0:1], off
	global_load_dwordx4 v[68:71], v[0:1], off offset:32
	global_load_dwordx4 v[72:75], v[0:1], off offset:64
	global_load_dwordx4 v[76:79], v[0:1], off offset:96
	v_add_u32_e32 v0, s42, v181
	v_mad_u64_u32 v[12:13], s[8:9], v0, s56, v[128:129]
	v_lshl_add_u32 v16, v0, 3, 0
	global_load_dwordx4 v[0:3], v[12:13], off offset:1024
	global_load_dwordx4 v[4:7], v[12:13], off offset:1056
	global_load_dwordx4 v[8:11], v[12:13], off offset:1088
	s_nop 0
	global_load_dwordx4 v[12:15], v[12:13], off offset:1120
	s_waitcnt vmcnt(4)
	v_and_b32_e32 v18, 0xffff0000, v64
	v_and_b32_e32 v20, 0xffff0000, v65
	v_lshlrev_b32_e32 v17, 16, v64
	v_lshlrev_b32_e32 v19, 16, v65
	v_and_b32_e32 v22, 0xffff0000, v66
	v_mul_f32_e32 v49, v18, v18
	v_mul_f32_e32 v50, v20, v20
	v_lshlrev_b32_e32 v21, 16, v66
	v_and_b32_e32 v24, 0xffff0000, v67
	v_mul_f32_e32 v51, v22, v22
	v_fmac_f32_e32 v49, v17, v17
	v_fmac_f32_e32 v50, v19, v19
	v_lshlrev_b32_e32 v23, 16, v67
	v_and_b32_e32 v26, 0xffff0000, v68
	v_mul_f32_e32 v52, v24, v24
	v_fmac_f32_e32 v51, v21, v21
	v_add_f32_e32 v49, v49, v50
	v_lshlrev_b32_e32 v25, 16, v68
	v_and_b32_e32 v28, 0xffff0000, v69
	v_mul_f32_e32 v53, v26, v26
	v_fmac_f32_e32 v52, v23, v23
	v_add_f32_e32 v49, v51, v49
	v_lshlrev_b32_e32 v27, 16, v69
	v_and_b32_e32 v30, 0xffff0000, v70
	v_mul_f32_e32 v54, v28, v28
	v_fmac_f32_e32 v53, v25, v25
	v_add_f32_e32 v49, v52, v49
	v_lshlrev_b32_e32 v29, 16, v70
	v_and_b32_e32 v32, 0xffff0000, v71
	v_mul_f32_e32 v55, v30, v30
	v_fmac_f32_e32 v54, v27, v27
	v_add_f32_e32 v49, v53, v49
	v_lshlrev_b32_e32 v31, 16, v71
	v_and_b32_e32 v34, 0xffff0000, v72
	v_mul_f32_e32 v56, v32, v32
	v_fmac_f32_e32 v55, v29, v29
	v_add_f32_e32 v49, v54, v49
	v_lshlrev_b32_e32 v33, 16, v72
	v_and_b32_e32 v36, 0xffff0000, v73
	v_mul_f32_e32 v57, v34, v34
	v_fmac_f32_e32 v56, v31, v31
	v_add_f32_e32 v49, v55, v49
	v_lshlrev_b32_e32 v35, 16, v73
	v_and_b32_e32 v38, 0xffff0000, v74
	v_mul_f32_e32 v58, v36, v36
	v_fmac_f32_e32 v57, v33, v33
	v_add_f32_e32 v49, v56, v49
	v_lshlrev_b32_e32 v37, 16, v74
	v_and_b32_e32 v40, 0xffff0000, v75
	v_mul_f32_e32 v59, v38, v38
	v_fmac_f32_e32 v58, v35, v35
	v_add_f32_e32 v49, v57, v49
	v_lshlrev_b32_e32 v39, 16, v75
	v_and_b32_e32 v42, 0xffff0000, v76
	v_mul_f32_e32 v60, v40, v40
	v_fmac_f32_e32 v59, v37, v37
	v_add_f32_e32 v49, v58, v49
	v_lshlrev_b32_e32 v41, 16, v76
	v_and_b32_e32 v44, 0xffff0000, v77
	v_mul_f32_e32 v61, v42, v42
	v_fmac_f32_e32 v60, v39, v39
	v_add_f32_e32 v49, v59, v49
	v_lshlrev_b32_e32 v43, 16, v77
	v_and_b32_e32 v46, 0xffff0000, v78
	v_mul_f32_e32 v62, v44, v44
	v_fmac_f32_e32 v61, v41, v41
	v_add_f32_e32 v49, v60, v49
	v_lshlrev_b32_e32 v45, 16, v78
	v_and_b32_e32 v48, 0xffff0000, v79
	v_mul_f32_e32 v63, v46, v46
	v_fmac_f32_e32 v62, v43, v43
	v_add_f32_e32 v49, v61, v49
	v_lshlrev_b32_e32 v47, 16, v79
	v_mul_f32_e32 v80, v48, v48
	v_fmac_f32_e32 v63, v45, v45
	v_add_f32_e32 v49, v62, v49
	v_fmac_f32_e32 v80, v47, v47
	v_add_f32_e32 v49, v63, v49
	v_add_f32_e32 v49, v80, v49
	v_mov_b32_e32 v50, v49
	s_nop 1
	v_permlane32_swap_b32_e32 v49, v50
	v_add_f32_e32 v49, v49, v50
	s_waitcnt vmcnt(3)
	v_lshlrev_b32_e32 v50, 16, v0
	v_and_b32_e32 v0, 0xffff0000, v0
	v_lshlrev_b32_e32 v51, 16, v1
	v_and_b32_e32 v1, 0xffff0000, v1
	v_mul_f32_e32 v0, v18, v0
	v_lshlrev_b32_e32 v52, 16, v2
	v_and_b32_e32 v2, 0xffff0000, v2
	v_mul_f32_e32 v1, v20, v1
	v_fmac_f32_e32 v0, v17, v50
	v_lshlrev_b32_e32 v53, 16, v3
	v_and_b32_e32 v3, 0xffff0000, v3
	v_mul_f32_e32 v2, v22, v2
	v_fmac_f32_e32 v1, v19, v51
	v_add_f32_e32 v0, 0, v0
	s_waitcnt vmcnt(2)
	v_lshlrev_b32_e32 v54, 16, v4
	v_and_b32_e32 v4, 0xffff0000, v4
	v_mul_f32_e32 v3, v24, v3
	v_fmac_f32_e32 v2, v21, v52
	v_add_f32_e32 v0, v1, v0
	v_lshlrev_b32_e32 v55, 16, v5
	v_and_b32_e32 v5, 0xffff0000, v5
	v_mul_f32_e32 v4, v26, v4
	v_fmac_f32_e32 v3, v23, v53
	v_add_f32_e32 v0, v2, v0
	v_lshlrev_b32_e32 v56, 16, v6
	v_and_b32_e32 v6, 0xffff0000, v6
	v_mul_f32_e32 v5, v28, v5
	v_fmac_f32_e32 v4, v25, v54
	v_add_f32_e32 v0, v3, v0
	v_lshlrev_b32_e32 v57, 16, v7
	v_and_b32_e32 v7, 0xffff0000, v7
	v_mul_f32_e32 v6, v30, v6
	v_fmac_f32_e32 v5, v27, v55
	v_add_f32_e32 v0, v4, v0
	s_waitcnt vmcnt(1)
	v_lshlrev_b32_e32 v58, 16, v8
	v_and_b32_e32 v8, 0xffff0000, v8
	v_mul_f32_e32 v7, v32, v7
	v_fmac_f32_e32 v6, v29, v56
	v_add_f32_e32 v0, v5, v0
	v_lshlrev_b32_e32 v59, 16, v9
	v_and_b32_e32 v9, 0xffff0000, v9
	v_mul_f32_e32 v8, v34, v8
	v_fmac_f32_e32 v7, v31, v57
	v_add_f32_e32 v0, v6, v0
	v_lshlrev_b32_e32 v60, 16, v10
	v_and_b32_e32 v10, 0xffff0000, v10
	v_mul_f32_e32 v9, v36, v9
	v_fmac_f32_e32 v8, v33, v58
	v_add_f32_e32 v0, v7, v0
	v_lshlrev_b32_e32 v61, 16, v11
	v_and_b32_e32 v11, 0xffff0000, v11
	v_mul_f32_e32 v10, v38, v10
	v_fmac_f32_e32 v9, v35, v59
	v_add_f32_e32 v0, v8, v0
	s_waitcnt vmcnt(0)
	v_lshlrev_b32_e32 v62, 16, v12
	v_and_b32_e32 v12, 0xffff0000, v12
	v_mul_f32_e32 v11, v40, v11
	v_fmac_f32_e32 v10, v37, v60
	v_add_f32_e32 v0, v9, v0
	v_lshlrev_b32_e32 v63, 16, v13
	v_and_b32_e32 v13, 0xffff0000, v13
	v_mul_f32_e32 v12, v42, v12
	v_fmac_f32_e32 v11, v39, v61
	v_add_f32_e32 v0, v10, v0
	v_lshlrev_b32_e32 v80, 16, v14
	v_and_b32_e32 v14, 0xffff0000, v14
	v_mul_f32_e32 v13, v44, v13
	v_fmac_f32_e32 v12, v41, v62
	v_add_f32_e32 v0, v11, v0
	v_lshlrev_b32_e32 v81, 16, v15
	v_and_b32_e32 v15, 0xffff0000, v15
	v_mul_f32_e32 v14, v46, v14
	v_fmac_f32_e32 v13, v43, v63
	v_add_f32_e32 v0, v12, v0
	v_mul_f32_e32 v15, v48, v15
	v_fmac_f32_e32 v14, v45, v80
	v_add_f32_e32 v0, v13, v0
	v_fmac_f32_e32 v15, v47, v81
	v_add_f32_e32 v0, v14, v0
	s_waitcnt vmcnt(0) lgkmcnt(0)
	s_barrier
	v_add_f32_e32 v2, v15, v0
	v_add_u32_e32 v0, 0x10000, v16
	ds_read_b64 v[0:1], v0
	v_mov_b32_e32 v3, v2
	s_nop 1
	v_permlane32_swap_b32_e32 v2, v3
	v_add_f32_e32 v2, v2, v3
	s_waitcnt lgkmcnt(0)
	v_lshlrev_b32_e32 v3, 16, v0
	v_and_b32_e32 v0, 0xffff0000, v0
	v_add_f32_e32 v0, v3, v0
	v_lshlrev_b32_e32 v1, 16, v1
	v_add_f32_e32 v0, v0, v1
	v_add_f32_e32 v0, v2, v0
	ds_bpermute_b32 v1, v182, v49
	ds_bpermute_b32 v2, v182, v0
	s_waitcnt lgkmcnt(1)
	v_max_f32_e32 v1, v1, v1
	s_waitcnt lgkmcnt(0)
	v_max_f32_e32 v2, v2, v2
	v_max_f32_e32 v1, v49, v1
	v_min_f32_e32 v0, v0, v2
	ds_bpermute_b32 v3, v183, v1
	ds_bpermute_b32 v2, v183, v0
	s_waitcnt lgkmcnt(1)
	v_max_f32_e32 v3, v3, v3
	s_waitcnt lgkmcnt(0)
	v_max_f32_e32 v2, v2, v2
	v_max_f32_e32 v1, v1, v3
	v_min_f32_e32 v0, v0, v2
	ds_bpermute_b32 v3, v184, v1
	ds_bpermute_b32 v2, v184, v0
	s_waitcnt lgkmcnt(1)
	v_max_f32_e32 v3, v3, v3
	s_waitcnt lgkmcnt(0)
	v_max_f32_e32 v2, v2, v2
	v_max_f32_e32 v1, v1, v3
	v_min_f32_e32 v0, v0, v2
	ds_bpermute_b32 v3, v185, v1
	ds_bpermute_b32 v2, v185, v0
	s_waitcnt lgkmcnt(1)
	v_max_f32_e32 v3, v3, v3
	s_waitcnt lgkmcnt(0)
	v_max_f32_e32 v2, v2, v2
	v_max_f32_e32 v1, v1, v3
	v_min_f32_e32 v0, v0, v2
	ds_bpermute_b32 v3, v186, v1
	ds_bpermute_b32 v2, v186, v0
	s_and_saveexec_b64 s[8:9], s[2:3]
	s_cbranch_execz .LBB0_277
	s_waitcnt lgkmcnt(1)
	v_max_f32_e32 v3, v3, v3
	v_max_f32_e32 v1, v1, v1
	s_waitcnt lgkmcnt(0)
	v_max_f32_e32 v2, v2, v2
	v_max_f32_e32 v0, v0, v0
	v_max_f32_e32 v1, v1, v3
	v_min_f32_e32 v0, v0, v2
	v_mov_b32_e32 v2, s59
	ds_write2_b32 v2, v1, v0 offset1:8
